# speedup vs baseline: 1.0024x; 1.0024x over previous
.Ldn_loop:
	s_waitcnt lgkmcnt(0)
	v_mfma_f32_16x16x32_bf16 v[64:67], v[176:179], v[160:163], v[64:67]
	ds_read_b128 v[200:203], v11 offset:0
	v_mfma_f32_16x16x32_bf16 v[68:71], v[176:179], v[164:167], v[68:71]
	s_add_u32 m0, s20, 0x5000
	v_mfma_f32_16x16x32_bf16 v[72:75], v[176:179], v[168:171], v[72:75]
	ds_read_b128 v[204:207], v11 offset:2048
	v_mfma_f32_16x16x32_bf16 v[76:79], v[176:179], v[172:175], v[76:79]
	global_load_lds_dwordx4 v3, s[18:19]
	v_mfma_f32_16x16x32_bf16 v[80:83], v[180:183], v[160:163], v[80:83]
	ds_read_b128 v[208:211], v11 offset:4096
	v_mfma_f32_16x16x32_bf16 v[84:87], v[180:183], v[164:167], v[84:87]
	s_add_u32 m0, s20, 0x6000
	v_mfma_f32_16x16x32_bf16 v[88:91], v[180:183], v[168:171], v[88:91]
	ds_read_b128 v[212:215], v11 offset:6144
	v_mfma_f32_16x16x32_bf16 v[92:95], v[180:183], v[172:175], v[92:95]
	global_load_lds_dwordx4 v4, s[18:19]
	v_mfma_f32_16x16x32_bf16 v[96:99], v[184:187], v[160:163], v[96:99]
	ds_read_b128 v[216:219], v13 offset:0
	v_mfma_f32_16x16x32_bf16 v[100:103], v[184:187], v[164:167], v[100:103]
	s_add_u32 m0, s20, 0x7000
	v_mfma_f32_16x16x32_bf16 v[104:107], v[184:187], v[168:171], v[104:107]
	ds_read_b128 v[220:223], v13 offset:2048
	v_mfma_f32_16x16x32_bf16 v[108:111], v[184:187], v[172:175], v[108:111]
	global_load_lds_dwordx4 v5, s[18:19]
	v_mfma_f32_16x16x32_bf16 v[112:115], v[188:191], v[160:163], v[112:115]
	ds_read_b128 v[224:227], v13 offset:4096
	v_mfma_f32_16x16x32_bf16 v[116:119], v[188:191], v[164:167], v[116:119]
	s_add_u32 m0, s20, 0x8000
	v_mfma_f32_16x16x32_bf16 v[120:123], v[188:191], v[168:171], v[120:123]
	ds_read_b128 v[228:231], v13 offset:6144
	v_mfma_f32_16x16x32_bf16 v[124:127], v[188:191], v[172:175], v[124:127]
	global_load_lds_dwordx4 v6, s[18:19]
	v_mfma_f32_16x16x32_bf16 v[128:131], v[192:195], v[160:163], v[128:131]
	ds_read_b128 v[232:235], v13 offset:8192
	v_mfma_f32_16x16x32_bf16 v[132:135], v[192:195], v[164:167], v[132:135]
	s_add_u32 m0, s20, 0x9000
	v_mfma_f32_16x16x32_bf16 v[136:139], v[192:195], v[168:171], v[136:139]
	ds_read_b128 v[236:239], v13 offset:10240
	v_mfma_f32_16x16x32_bf16 v[140:143], v[192:195], v[172:175], v[140:143]
	global_load_lds_dwordx4 v7, s[18:19]
	v_mfma_f32_16x16x32_bf16 v[144:147], v[196:199], v[160:163], v[144:147]
	s_add_u32 s16, s16, 0x80
	s_addc_u32 s17, s17, 0
	s_add_u32 s18, s18, 0x80
	s_addc_u32 s19, s19, 0
	v_mfma_f32_16x16x32_bf16 v[148:151], v[196:199], v[164:167], v[148:151]
	s_add_u32 s20, s20, 0xa000
	s_sub_u32 s22, s20, 0x28000
	s_cmp_ge_u32 s20, 0x28000
	s_cselect_b32 s20, s22, s20
	v_mfma_f32_16x16x32_bf16 v[152:155], v[196:199], v[168:171], v[152:155]
	v_add_u32_e32 v10, s21, v8
	v_add_u32_e32 v12, s21, v9
	v_xor_b32_e32 v11, 64, v10
	v_xor_b32_e32 v13, 64, v12
	v_mfma_f32_16x16x32_bf16 v[156:159], v[196:199], v[172:175], v[156:159]
	s_add_u32 s21, s21, 0xa000
	s_sub_u32 s23, s21, 0x28000
	s_cmp_ge_u32 s21, 0x28000
	s_cselect_b32 s21, s23, s21
	s_waitcnt lgkmcnt(0)
	v_mfma_f32_16x16x32_bf16 v[64:67], v[216:219], v[200:203], v[64:67]
	v_mfma_f32_16x16x32_bf16 v[68:71], v[216:219], v[204:207], v[68:71]
	v_mfma_f32_16x16x32_bf16 v[72:75], v[216:219], v[208:211], v[72:75]
	v_mfma_f32_16x16x32_bf16 v[76:79], v[216:219], v[212:215], v[76:79]
	s_waitcnt vmcnt(20)
	s_barrier
	v_mfma_f32_16x16x32_bf16 v[80:83], v[220:223], v[200:203], v[80:83]
	ds_read_b128 v[160:163], v10 offset:0
	v_mfma_f32_16x16x32_bf16 v[84:87], v[220:223], v[204:207], v[84:87]
	s_add_u32 m0, s20, 0x0
	v_mfma_f32_16x16x32_bf16 v[88:91], v[220:223], v[208:211], v[88:91]
	ds_read_b128 v[164:167], v10 offset:2048
	v_mfma_f32_16x16x32_bf16 v[92:95], v[220:223], v[212:215], v[92:95]
	global_load_lds_dwordx4 v2, s[16:17]
	v_mfma_f32_16x16x32_bf16 v[96:99], v[224:227], v[200:203], v[96:99]
	ds_read_b128 v[168:171], v10 offset:4096
	v_mfma_f32_16x16x32_bf16 v[100:103], v[224:227], v[204:207], v[100:103]
	s_add_u32 m0, s20, 0x1000
	v_mfma_f32_16x16x32_bf16 v[104:107], v[224:227], v[208:211], v[104:107]
	ds_read_b128 v[172:175], v10 offset:6144
	v_mfma_f32_16x16x32_bf16 v[108:111], v[224:227], v[212:215], v[108:111]
	global_load_lds_dwordx4 v3, s[16:17]
	v_mfma_f32_16x16x32_bf16 v[112:115], v[228:231], v[200:203], v[112:115]
	ds_read_b128 v[176:179], v12 offset:0
	v_mfma_f32_16x16x32_bf16 v[116:119], v[228:231], v[204:207], v[116:119]
	s_add_u32 m0, s20, 0x2000
	v_mfma_f32_16x16x32_bf16 v[120:123], v[228:231], v[208:211], v[120:123]
	ds_read_b128 v[180:183], v12 offset:2048
	v_mfma_f32_16x16x32_bf16 v[124:127], v[228:231], v[212:215], v[124:127]
	global_load_lds_dwordx4 v4, s[16:17]
	v_mfma_f32_16x16x32_bf16 v[128:131], v[232:235], v[200:203], v[128:131]
	ds_read_b128 v[184:187], v12 offset:4096
	v_mfma_f32_16x16x32_bf16 v[132:135], v[232:235], v[204:207], v[132:135]
	s_add_u32 m0, s20, 0x3000
	v_mfma_f32_16x16x32_bf16 v[136:139], v[232:235], v[208:211], v[136:139]
	ds_read_b128 v[188:191], v12 offset:6144
	v_mfma_f32_16x16x32_bf16 v[140:143], v[232:235], v[212:215], v[140:143]
	global_load_lds_dwordx4 v5, s[16:17]
	v_mfma_f32_16x16x32_bf16 v[144:147], v[236:239], v[200:203], v[144:147]
	ds_read_b128 v[192:195], v12 offset:8192
	v_mfma_f32_16x16x32_bf16 v[148:151], v[236:239], v[204:207], v[148:151]
	s_add_u32 m0, s20, 0x4000
	v_mfma_f32_16x16x32_bf16 v[152:155], v[236:239], v[208:211], v[152:155]
	ds_read_b128 v[196:199], v12 offset:10240
	v_mfma_f32_16x16x32_bf16 v[156:159], v[236:239], v[212:215], v[156:159]
	global_load_lds_dwordx4 v2, s[18:19]
	s_add_u32 s15, s15, 1
	s_cmp_lt_u32 s15, 44
	s_cbranch_scc1 .Ldn_loop
	s_waitcnt lgkmcnt(0)
	v_mfma_f32_16x16x32_bf16 v[64:67], v[176:179], v[160:163], v[64:67]
	ds_read_b128 v[200:203], v11 offset:0
	v_mfma_f32_16x16x32_bf16 v[68:71], v[176:179], v[164:167], v[68:71]
	s_add_u32 m0, s20, 0x5000
	v_mfma_f32_16x16x32_bf16 v[72:75], v[176:179], v[168:171], v[72:75]
	ds_read_b128 v[204:207], v11 offset:2048
	v_mfma_f32_16x16x32_bf16 v[76:79], v[176:179], v[172:175], v[76:79]
	global_load_lds_dwordx4 v3, s[18:19]
	v_mfma_f32_16x16x32_bf16 v[80:83], v[180:183], v[160:163], v[80:83]
	ds_read_b128 v[208:211], v11 offset:4096
	v_mfma_f32_16x16x32_bf16 v[84:87], v[180:183], v[164:167], v[84:87]
	s_add_u32 m0, s20, 0x6000
	v_mfma_f32_16x16x32_bf16 v[88:91], v[180:183], v[168:171], v[88:91]
	ds_read_b128 v[212:215], v11 offset:6144
	v_mfma_f32_16x16x32_bf16 v[92:95], v[180:183], v[172:175], v[92:95]
	global_load_lds_dwordx4 v4, s[18:19]
	v_mfma_f32_16x16x32_bf16 v[96:99], v[184:187], v[160:163], v[96:99]
	ds_read_b128 v[216:219], v13 offset:0
	v_mfma_f32_16x16x32_bf16 v[100:103], v[184:187], v[164:167], v[100:103]
	s_add_u32 m0, s20, 0x7000
	v_mfma_f32_16x16x32_bf16 v[104:107], v[184:187], v[168:171], v[104:107]
	ds_read_b128 v[220:223], v13 offset:2048
	v_mfma_f32_16x16x32_bf16 v[108:111], v[184:187], v[172:175], v[108:111]
	global_load_lds_dwordx4 v5, s[18:19]
	v_mfma_f32_16x16x32_bf16 v[112:115], v[188:191], v[160:163], v[112:115]
	ds_read_b128 v[224:227], v13 offset:4096
	v_mfma_f32_16x16x32_bf16 v[116:119], v[188:191], v[164:167], v[116:119]
	s_add_u32 m0, s20, 0x8000
	v_mfma_f32_16x16x32_bf16 v[120:123], v[188:191], v[168:171], v[120:123]
	ds_read_b128 v[228:231], v13 offset:6144
	v_mfma_f32_16x16x32_bf16 v[124:127], v[188:191], v[172:175], v[124:127]
	global_load_lds_dwordx4 v6, s[18:19]
	v_mfma_f32_16x16x32_bf16 v[128:131], v[192:195], v[160:163], v[128:131]
	ds_read_b128 v[232:235], v13 offset:8192
	v_mfma_f32_16x16x32_bf16 v[132:135], v[192:195], v[164:167], v[132:135]
	s_add_u32 m0, s20, 0x9000
	v_mfma_f32_16x16x32_bf16 v[136:139], v[192:195], v[168:171], v[136:139]
	ds_read_b128 v[236:239], v13 offset:10240
	v_mfma_f32_16x16x32_bf16 v[140:143], v[192:195], v[172:175], v[140:143]
	global_load_lds_dwordx4 v7, s[18:19]
	v_mfma_f32_16x16x32_bf16 v[144:147], v[196:199], v[160:163], v[144:147]
	s_add_u32 s16, s16, 0x80
	s_addc_u32 s17, s17, 0
	s_add_u32 s18, s18, 0x80
	s_addc_u32 s19, s19, 0
	v_mfma_f32_16x16x32_bf16 v[148:151], v[196:199], v[164:167], v[148:151]
	s_add_u32 s20, s20, 0xa000
	s_sub_u32 s22, s20, 0x28000
	s_cmp_ge_u32 s20, 0x28000
	s_cselect_b32 s20, s22, s20
	v_mfma_f32_16x16x32_bf16 v[152:155], v[196:199], v[168:171], v[152:155]
	v_add_u32_e32 v10, s21, v8
	v_add_u32_e32 v12, s21, v9
	v_xor_b32_e32 v11, 64, v10
	v_xor_b32_e32 v13, 64, v12
	v_mfma_f32_16x16x32_bf16 v[156:159], v[196:199], v[172:175], v[156:159]
	s_add_u32 s21, s21, 0xa000
	s_sub_u32 s23, s21, 0x28000
	s_cmp_ge_u32 s21, 0x28000
	s_cselect_b32 s21, s23, s21
	s_waitcnt lgkmcnt(0)
	v_mfma_f32_16x16x32_bf16 v[64:67], v[216:219], v[200:203], v[64:67]
	v_mfma_f32_16x16x32_bf16 v[68:71], v[216:219], v[204:207], v[68:71]
	v_mfma_f32_16x16x32_bf16 v[72:75], v[216:219], v[208:211], v[72:75]
	v_mfma_f32_16x16x32_bf16 v[76:79], v[216:219], v[212:215], v[76:79]
	s_waitcnt vmcnt(20)
	s_barrier
	v_mfma_f32_16x16x32_bf16 v[80:83], v[220:223], v[200:203], v[80:83]
	ds_read_b128 v[160:163], v10 offset:0
	v_mfma_f32_16x16x32_bf16 v[84:87], v[220:223], v[204:207], v[84:87]
	ds_read_b128 v[164:167], v10 offset:2048
	v_mfma_f32_16x16x32_bf16 v[88:91], v[220:223], v[208:211], v[88:91]
	ds_read_b128 v[168:171], v10 offset:4096
	v_mfma_f32_16x16x32_bf16 v[92:95], v[220:223], v[212:215], v[92:95]
	ds_read_b128 v[172:175], v10 offset:6144
	v_mfma_f32_16x16x32_bf16 v[96:99], v[224:227], v[200:203], v[96:99]
	ds_read_b128 v[176:179], v12 offset:0
	v_mfma_f32_16x16x32_bf16 v[100:103], v[224:227], v[204:207], v[100:103]
	ds_read_b128 v[180:183], v12 offset:2048
	v_mfma_f32_16x16x32_bf16 v[104:107], v[224:227], v[208:211], v[104:107]
	ds_read_b128 v[184:187], v12 offset:4096
	v_mfma_f32_16x16x32_bf16 v[108:111], v[224:227], v[212:215], v[108:111]
	ds_read_b128 v[188:191], v12 offset:6144
	v_mfma_f32_16x16x32_bf16 v[112:115], v[228:231], v[200:203], v[112:115]
	ds_read_b128 v[192:195], v12 offset:8192
	v_mfma_f32_16x16x32_bf16 v[116:119], v[228:231], v[204:207], v[116:119]
	ds_read_b128 v[196:199], v12 offset:10240
	v_mfma_f32_16x16x32_bf16 v[120:123], v[228:231], v[208:211], v[120:123]
	v_mfma_f32_16x16x32_bf16 v[124:127], v[228:231], v[212:215], v[124:127]
	v_mfma_f32_16x16x32_bf16 v[128:131], v[232:235], v[200:203], v[128:131]
	v_mfma_f32_16x16x32_bf16 v[132:135], v[232:235], v[204:207], v[132:135]
	v_mfma_f32_16x16x32_bf16 v[136:139], v[232:235], v[208:211], v[136:139]
	v_mfma_f32_16x16x32_bf16 v[140:143], v[232:235], v[212:215], v[140:143]
	v_mfma_f32_16x16x32_bf16 v[144:147], v[236:239], v[200:203], v[144:147]
	v_mfma_f32_16x16x32_bf16 v[148:151], v[236:239], v[204:207], v[148:151]
	v_mfma_f32_16x16x32_bf16 v[152:155], v[236:239], v[208:211], v[152:155]
	v_mfma_f32_16x16x32_bf16 v[156:159], v[236:239], v[212:215], v[156:159]
	s_waitcnt lgkmcnt(0)
	v_mfma_f32_16x16x32_bf16 v[64:67], v[176:179], v[160:163], v[64:67]
	ds_read_b128 v[200:203], v11 offset:0
	v_mfma_f32_16x16x32_bf16 v[68:71], v[176:179], v[164:167], v[68:71]
	ds_read_b128 v[204:207], v11 offset:2048
	v_mfma_f32_16x16x32_bf16 v[72:75], v[176:179], v[168:171], v[72:75]
	ds_read_b128 v[208:211], v11 offset:4096
	v_mfma_f32_16x16x32_bf16 v[76:79], v[176:179], v[172:175], v[76:79]
	ds_read_b128 v[212:215], v11 offset:6144
	v_mfma_f32_16x16x32_bf16 v[80:83], v[180:183], v[160:163], v[80:83]
	ds_read_b128 v[216:219], v13 offset:0
	v_mfma_f32_16x16x32_bf16 v[84:87], v[180:183], v[164:167], v[84:87]
	ds_read_b128 v[220:223], v13 offset:2048
	v_mfma_f32_16x16x32_bf16 v[88:91], v[180:183], v[168:171], v[88:91]
	ds_read_b128 v[224:227], v13 offset:4096
	v_mfma_f32_16x16x32_bf16 v[92:95], v[180:183], v[172:175], v[92:95]
	ds_read_b128 v[228:231], v13 offset:6144
	v_mfma_f32_16x16x32_bf16 v[96:99], v[184:187], v[160:163], v[96:99]
	ds_read_b128 v[232:235], v13 offset:8192
	v_mfma_f32_16x16x32_bf16 v[100:103], v[184:187], v[164:167], v[100:103]
	ds_read_b128 v[236:239], v13 offset:10240
	v_mfma_f32_16x16x32_bf16 v[104:107], v[184:187], v[168:171], v[104:107]
	v_mfma_f32_16x16x32_bf16 v[108:111], v[184:187], v[172:175], v[108:111]
	v_mfma_f32_16x16x32_bf16 v[112:115], v[188:191], v[160:163], v[112:115]
	v_mfma_f32_16x16x32_bf16 v[116:119], v[188:191], v[164:167], v[116:119]
	v_mfma_f32_16x16x32_bf16 v[120:123], v[188:191], v[168:171], v[120:123]
	v_mfma_f32_16x16x32_bf16 v[124:127], v[188:191], v[172:175], v[124:127]
	v_mfma_f32_16x16x32_bf16 v[128:131], v[192:195], v[160:163], v[128:131]
	v_mfma_f32_16x16x32_bf16 v[132:135], v[192:195], v[164:167], v[132:135]
	v_mfma_f32_16x16x32_bf16 v[136:139], v[192:195], v[168:171], v[136:139]
	v_mfma_f32_16x16x32_bf16 v[140:143], v[192:195], v[172:175], v[140:143]
	v_mfma_f32_16x16x32_bf16 v[144:147], v[196:199], v[160:163], v[144:147]
	v_add_u32_e32 v10, s21, v8
	v_add_u32_e32 v12, s21, v9
	v_xor_b32_e32 v11, 64, v10
	v_xor_b32_e32 v13, 64, v12
	v_mfma_f32_16x16x32_bf16 v[148:151], v[196:199], v[164:167], v[148:151]
	s_add_u32 s21, s21, 0xa000
	s_sub_u32 s23, s21, 0x28000
	s_cmp_ge_u32 s21, 0x28000
	s_cselect_b32 s21, s23, s21
	v_mfma_f32_16x16x32_bf16 v[152:155], v[196:199], v[168:171], v[152:155]
	v_mfma_f32_16x16x32_bf16 v[156:159], v[196:199], v[172:175], v[156:159]
	s_waitcnt lgkmcnt(0)
	v_mfma_f32_16x16x32_bf16 v[64:67], v[216:219], v[200:203], v[64:67]
	v_mfma_f32_16x16x32_bf16 v[68:71], v[216:219], v[204:207], v[68:71]
	v_mfma_f32_16x16x32_bf16 v[72:75], v[216:219], v[208:211], v[72:75]
	v_mfma_f32_16x16x32_bf16 v[76:79], v[216:219], v[212:215], v[76:79]
	s_waitcnt vmcnt(10)
	s_barrier
	v_mfma_f32_16x16x32_bf16 v[80:83], v[220:223], v[200:203], v[80:83]
	ds_read_b128 v[160:163], v10 offset:0
	v_mfma_f32_16x16x32_bf16 v[84:87], v[220:223], v[204:207], v[84:87]
	ds_read_b128 v[164:167], v10 offset:2048
	v_mfma_f32_16x16x32_bf16 v[88:91], v[220:223], v[208:211], v[88:91]
	ds_read_b128 v[168:171], v10 offset:4096
	v_mfma_f32_16x16x32_bf16 v[92:95], v[220:223], v[212:215], v[92:95]
	ds_read_b128 v[172:175], v10 offset:6144
	v_mfma_f32_16x16x32_bf16 v[96:99], v[224:227], v[200:203], v[96:99]
	ds_read_b128 v[176:179], v12 offset:0
	v_mfma_f32_16x16x32_bf16 v[100:103], v[224:227], v[204:207], v[100:103]
	ds_read_b128 v[180:183], v12 offset:2048
	v_mfma_f32_16x16x32_bf16 v[104:107], v[224:227], v[208:211], v[104:107]
	ds_read_b128 v[184:187], v12 offset:4096
	v_mfma_f32_16x16x32_bf16 v[108:111], v[224:227], v[212:215], v[108:111]
	ds_read_b128 v[188:191], v12 offset:6144
	v_mfma_f32_16x16x32_bf16 v[112:115], v[228:231], v[200:203], v[112:115]
	ds_read_b128 v[192:195], v12 offset:8192
	v_mfma_f32_16x16x32_bf16 v[116:119], v[228:231], v[204:207], v[116:119]
	ds_read_b128 v[196:199], v12 offset:10240
	v_mfma_f32_16x16x32_bf16 v[120:123], v[228:231], v[208:211], v[120:123]
	v_mfma_f32_16x16x32_bf16 v[124:127], v[228:231], v[212:215], v[124:127]
	v_mfma_f32_16x16x32_bf16 v[128:131], v[232:235], v[200:203], v[128:131]
	v_mfma_f32_16x16x32_bf16 v[132:135], v[232:235], v[204:207], v[132:135]
	v_mfma_f32_16x16x32_bf16 v[136:139], v[232:235], v[208:211], v[136:139]
	v_mfma_f32_16x16x32_bf16 v[140:143], v[232:235], v[212:215], v[140:143]
	v_mfma_f32_16x16x32_bf16 v[144:147], v[236:239], v[200:203], v[144:147]
	v_mfma_f32_16x16x32_bf16 v[148:151], v[236:239], v[204:207], v[148:151]
	v_mfma_f32_16x16x32_bf16 v[152:155], v[236:239], v[208:211], v[152:155]
	v_mfma_f32_16x16x32_bf16 v[156:159], v[236:239], v[212:215], v[156:159]
	s_waitcnt lgkmcnt(0)
	v_mfma_f32_16x16x32_bf16 v[64:67], v[176:179], v[160:163], v[64:67]
	ds_read_b128 v[200:203], v11 offset:0
	v_mfma_f32_16x16x32_bf16 v[68:71], v[176:179], v[164:167], v[68:71]
	ds_read_b128 v[204:207], v11 offset:2048
	v_mfma_f32_16x16x32_bf16 v[72:75], v[176:179], v[168:171], v[72:75]
	ds_read_b128 v[208:211], v11 offset:4096
	v_mfma_f32_16x16x32_bf16 v[76:79], v[176:179], v[172:175], v[76:79]
	ds_read_b128 v[212:215], v11 offset:6144
	v_mfma_f32_16x16x32_bf16 v[80:83], v[180:183], v[160:163], v[80:83]
	ds_read_b128 v[216:219], v13 offset:0
	v_mfma_f32_16x16x32_bf16 v[84:87], v[180:183], v[164:167], v[84:87]
	ds_read_b128 v[220:223], v13 offset:2048
	v_mfma_f32_16x16x32_bf16 v[88:91], v[180:183], v[168:171], v[88:91]
	ds_read_b128 v[224:227], v13 offset:4096
	v_mfma_f32_16x16x32_bf16 v[92:95], v[180:183], v[172:175], v[92:95]
	ds_read_b128 v[228:231], v13 offset:6144
	v_mfma_f32_16x16x32_bf16 v[96:99], v[184:187], v[160:163], v[96:99]
	ds_read_b128 v[232:235], v13 offset:8192
	v_mfma_f32_16x16x32_bf16 v[100:103], v[184:187], v[164:167], v[100:103]
	ds_read_b128 v[236:239], v13 offset:10240
	v_mfma_f32_16x16x32_bf16 v[104:107], v[184:187], v[168:171], v[104:107]
	v_mfma_f32_16x16x32_bf16 v[108:111], v[184:187], v[172:175], v[108:111]
	v_mfma_f32_16x16x32_bf16 v[112:115], v[188:191], v[160:163], v[112:115]
	v_mfma_f32_16x16x32_bf16 v[116:119], v[188:191], v[164:167], v[116:119]
	v_mfma_f32_16x16x32_bf16 v[120:123], v[188:191], v[168:171], v[120:123]
	v_mfma_f32_16x16x32_bf16 v[124:127], v[188:191], v[172:175], v[124:127]
	v_mfma_f32_16x16x32_bf16 v[128:131], v[192:195], v[160:163], v[128:131]
	v_mfma_f32_16x16x32_bf16 v[132:135], v[192:195], v[164:167], v[132:135]
	v_mfma_f32_16x16x32_bf16 v[136:139], v[192:195], v[168:171], v[136:139]
	v_mfma_f32_16x16x32_bf16 v[140:143], v[192:195], v[172:175], v[140:143]
	v_mfma_f32_16x16x32_bf16 v[144:147], v[196:199], v[160:163], v[144:147]
	v_add_u32_e32 v10, s21, v8
	v_add_u32_e32 v12, s21, v9
	v_xor_b32_e32 v11, 64, v10
	v_xor_b32_e32 v13, 64, v12
	v_mfma_f32_16x16x32_bf16 v[148:151], v[196:199], v[164:167], v[148:151]
	s_add_u32 s21, s21, 0xa000
	s_sub_u32 s23, s21, 0x28000
	s_cmp_ge_u32 s21, 0x28000
	s_cselect_b32 s21, s23, s21
	v_mfma_f32_16x16x32_bf16 v[152:155], v[196:199], v[168:171], v[152:155]
	v_mfma_f32_16x16x32_bf16 v[156:159], v[196:199], v[172:175], v[156:159]
	s_waitcnt lgkmcnt(0)
	v_mfma_f32_16x16x32_bf16 v[64:67], v[216:219], v[200:203], v[64:67]
	v_mfma_f32_16x16x32_bf16 v[68:71], v[216:219], v[204:207], v[68:71]
	v_mfma_f32_16x16x32_bf16 v[72:75], v[216:219], v[208:211], v[72:75]
	v_mfma_f32_16x16x32_bf16 v[76:79], v[216:219], v[212:215], v[76:79]
	s_waitcnt vmcnt(0)
	s_barrier
	v_mfma_f32_16x16x32_bf16 v[80:83], v[220:223], v[200:203], v[80:83]
	ds_read_b128 v[160:163], v10 offset:0
	v_mfma_f32_16x16x32_bf16 v[84:87], v[220:223], v[204:207], v[84:87]
	global_load_dwordx4 v[16:19], v56, s[8:9] offset:0
	v_mfma_f32_16x16x32_bf16 v[88:91], v[220:223], v[208:211], v[88:91]
	ds_read_b128 v[164:167], v10 offset:2048
	v_mfma_f32_16x16x32_bf16 v[92:95], v[220:223], v[212:215], v[92:95]
	global_load_dwordx4 v[20:23], v57, s[8:9] offset:0
	v_mfma_f32_16x16x32_bf16 v[96:99], v[224:227], v[200:203], v[96:99]
	ds_read_b128 v[168:171], v10 offset:4096
	v_mfma_f32_16x16x32_bf16 v[100:103], v[224:227], v[204:207], v[100:103]
	global_load_dwordx4 v[24:27], v58, s[8:9] offset:0
	v_mfma_f32_16x16x32_bf16 v[104:107], v[224:227], v[208:211], v[104:107]
	ds_read_b128 v[172:175], v10 offset:6144
	v_mfma_f32_16x16x32_bf16 v[108:111], v[224:227], v[212:215], v[108:111]
	global_load_dwordx4 v[28:31], v59, s[8:9] offset:0
	v_mfma_f32_16x16x32_bf16 v[112:115], v[228:231], v[200:203], v[112:115]
	ds_read_b128 v[176:179], v12 offset:0
	v_mfma_f32_16x16x32_bf16 v[116:119], v[228:231], v[204:207], v[116:119]
	global_load_dwordx4 v[32:35], v56, s[8:9] offset:64
	v_mfma_f32_16x16x32_bf16 v[120:123], v[228:231], v[208:211], v[120:123]
	ds_read_b128 v[180:183], v12 offset:2048
	v_mfma_f32_16x16x32_bf16 v[124:127], v[228:231], v[212:215], v[124:127]
	global_load_dwordx4 v[36:39], v57, s[8:9] offset:64
	v_mfma_f32_16x16x32_bf16 v[128:131], v[232:235], v[200:203], v[128:131]
	ds_read_b128 v[184:187], v12 offset:4096
	v_mfma_f32_16x16x32_bf16 v[132:135], v[232:235], v[204:207], v[132:135]
	global_load_dwordx4 v[40:43], v58, s[8:9] offset:64
	v_mfma_f32_16x16x32_bf16 v[136:139], v[232:235], v[208:211], v[136:139]
	ds_read_b128 v[188:191], v12 offset:6144
	v_mfma_f32_16x16x32_bf16 v[140:143], v[232:235], v[212:215], v[140:143]
	global_load_dwordx4 v[44:47], v59, s[8:9] offset:64
	v_mfma_f32_16x16x32_bf16 v[144:147], v[236:239], v[200:203], v[144:147]
	ds_read_b128 v[192:195], v12 offset:8192
	v_mfma_f32_16x16x32_bf16 v[148:151], v[236:239], v[204:207], v[148:151]
	global_load_dwordx4 v[48:51], v56, s[8:9] offset:128
	v_mfma_f32_16x16x32_bf16 v[152:155], v[236:239], v[208:211], v[152:155]
	ds_read_b128 v[196:199], v12 offset:10240
	v_mfma_f32_16x16x32_bf16 v[156:159], v[236:239], v[212:215], v[156:159]
	global_load_dwordx4 v[52:55], v57, s[8:9] offset:128
	global_load_dwordx4 v[240:243], v58, s[8:9] offset:128
	global_load_dwordx4 v[244:247], v59, s[8:9] offset:128
	global_load_dwordx4 v[248:251], v56, s[8:9] offset:192
	global_load_dwordx4 v[252:255], v57, s[8:9] offset:192
	s_waitcnt lgkmcnt(0)
	v_mfma_f32_16x16x32_bf16 v[64:67], v[176:179], v[160:163], v[64:67]
	ds_read_b128 v[200:203], v11 offset:0
	v_mfma_f32_16x16x32_bf16 v[68:71], v[176:179], v[164:167], v[68:71]
	ds_read_b128 v[204:207], v11 offset:2048
	v_mfma_f32_16x16x32_bf16 v[72:75], v[176:179], v[168:171], v[72:75]
	ds_read_b128 v[208:211], v11 offset:4096
	v_mfma_f32_16x16x32_bf16 v[76:79], v[176:179], v[172:175], v[76:79]
	ds_read_b128 v[212:215], v11 offset:6144
	v_mfma_f32_16x16x32_bf16 v[80:83], v[180:183], v[160:163], v[80:83]
	ds_read_b128 v[216:219], v13 offset:0
	v_mfma_f32_16x16x32_bf16 v[84:87], v[180:183], v[164:167], v[84:87]
	ds_read_b128 v[220:223], v13 offset:2048
	v_mfma_f32_16x16x32_bf16 v[88:91], v[180:183], v[168:171], v[88:91]
	ds_read_b128 v[224:227], v13 offset:4096
	v_mfma_f32_16x16x32_bf16 v[92:95], v[180:183], v[172:175], v[92:95]
	ds_read_b128 v[228:231], v13 offset:6144
	v_mfma_f32_16x16x32_bf16 v[96:99], v[184:187], v[160:163], v[96:99]
	ds_read_b128 v[232:235], v13 offset:8192
	v_mfma_f32_16x16x32_bf16 v[100:103], v[184:187], v[164:167], v[100:103]
	ds_read_b128 v[236:239], v13 offset:10240
	v_mfma_f32_16x16x32_bf16 v[104:107], v[184:187], v[168:171], v[104:107]
	v_mfma_f32_16x16x32_bf16 v[108:111], v[184:187], v[172:175], v[108:111]
	v_mfma_f32_16x16x32_bf16 v[112:115], v[188:191], v[160:163], v[112:115]
	v_mfma_f32_16x16x32_bf16 v[116:119], v[188:191], v[164:167], v[116:119]
	v_mfma_f32_16x16x32_bf16 v[120:123], v[188:191], v[168:171], v[120:123]
	v_mfma_f32_16x16x32_bf16 v[124:127], v[188:191], v[172:175], v[124:127]
	v_mfma_f32_16x16x32_bf16 v[128:131], v[192:195], v[160:163], v[128:131]
	v_mfma_f32_16x16x32_bf16 v[132:135], v[192:195], v[164:167], v[132:135]
	v_mfma_f32_16x16x32_bf16 v[136:139], v[192:195], v[168:171], v[136:139]
	v_mfma_f32_16x16x32_bf16 v[140:143], v[192:195], v[172:175], v[140:143]
	v_mfma_f32_16x16x32_bf16 v[144:147], v[196:199], v[160:163], v[144:147]
	v_mfma_f32_16x16x32_bf16 v[148:151], v[196:199], v[164:167], v[148:151]
	v_mfma_f32_16x16x32_bf16 v[152:155], v[196:199], v[168:171], v[152:155]
	v_mfma_f32_16x16x32_bf16 v[156:159], v[196:199], v[172:175], v[156:159]
	s_waitcnt lgkmcnt(0)
	v_mfma_f32_16x16x32_bf16 v[64:67], v[216:219], v[200:203], v[64:67]
	v_mfma_f32_16x16x32_bf16 v[68:71], v[216:219], v[204:207], v[68:71]
	global_load_dwordx4 v[160:163], v58, s[8:9] offset:192
	v_mfma_f32_16x16x32_bf16 v[72:75], v[216:219], v[208:211], v[72:75]
	v_mfma_f32_16x16x32_bf16 v[76:79], v[216:219], v[212:215], v[76:79]
	global_load_dwordx4 v[164:167], v59, s[8:9] offset:192
	v_mfma_f32_16x16x32_bf16 v[80:83], v[220:223], v[200:203], v[80:83]
	v_mfma_f32_16x16x32_bf16 v[84:87], v[220:223], v[204:207], v[84:87]
	global_load_dwordx4 v[168:171], v56, s[8:9] offset:256
	v_mfma_f32_16x16x32_bf16 v[88:91], v[220:223], v[208:211], v[88:91]
	v_mfma_f32_16x16x32_bf16 v[92:95], v[220:223], v[212:215], v[92:95]
	global_load_dwordx4 v[172:175], v57, s[8:9] offset:256
	v_mfma_f32_16x16x32_bf16 v[96:99], v[224:227], v[200:203], v[96:99]
	v_mfma_f32_16x16x32_bf16 v[100:103], v[224:227], v[204:207], v[100:103]
	global_load_dwordx4 v[176:179], v58, s[8:9] offset:256
	v_mfma_f32_16x16x32_bf16 v[104:107], v[224:227], v[208:211], v[104:107]
	v_mfma_f32_16x16x32_bf16 v[108:111], v[224:227], v[212:215], v[108:111]
	global_load_dwordx4 v[180:183], v59, s[8:9] offset:256
	v_mfma_f32_16x16x32_bf16 v[112:115], v[228:231], v[200:203], v[112:115]
	v_mfma_f32_16x16x32_bf16 v[116:119], v[228:231], v[204:207], v[116:119]
	global_load_dwordx4 v[184:187], v56, s[8:9] offset:320
	v_mfma_f32_16x16x32_bf16 v[120:123], v[228:231], v[208:211], v[120:123]
	v_mfma_f32_16x16x32_bf16 v[124:127], v[228:231], v[212:215], v[124:127]
	global_load_dwordx4 v[188:191], v57, s[8:9] offset:320
	v_mfma_f32_16x16x32_bf16 v[128:131], v[232:235], v[200:203], v[128:131]
	v_mfma_f32_16x16x32_bf16 v[132:135], v[232:235], v[204:207], v[132:135]
	global_load_dwordx4 v[192:195], v58, s[8:9] offset:320
	v_mfma_f32_16x16x32_bf16 v[136:139], v[232:235], v[208:211], v[136:139]
	v_mfma_f32_16x16x32_bf16 v[140:143], v[232:235], v[212:215], v[140:143]
	global_load_dwordx4 v[196:199], v59, s[8:9] offset:320
	v_mfma_f32_16x16x32_bf16 v[144:147], v[236:239], v[200:203], v[144:147]
	v_mfma_f32_16x16x32_bf16 v[148:151], v[236:239], v[204:207], v[148:151]
	v_mfma_f32_16x16x32_bf16 v[152:155], v[236:239], v[208:211], v[152:155]
	v_mfma_f32_16x16x32_bf16 v[156:159], v[236:239], v[212:215], v[156:159]
	s_waitcnt vmcnt(23)
	v_pk_add_f32 v[64:65], v[64:65], v[16:17]
	v_pk_add_f32 v[66:67], v[66:67], v[18:19]
	global_store_dwordx4 v56, v[64:67], s[10:11] offset:0 sc0 sc1
	s_waitcnt vmcnt(23)
	v_pk_add_f32 v[68:69], v[68:69], v[20:21]
	v_pk_add_f32 v[70:71], v[70:71], v[22:23]
	global_store_dwordx4 v57, v[68:71], s[10:11] offset:0 sc0 sc1
	s_waitcnt vmcnt(23)
	v_pk_add_f32 v[72:73], v[72:73], v[24:25]
	v_pk_add_f32 v[74:75], v[74:75], v[26:27]
	global_store_dwordx4 v58, v[72:75], s[10:11] offset:0 sc0 sc1
	s_waitcnt vmcnt(23)
	v_pk_add_f32 v[76:77], v[76:77], v[28:29]
	v_pk_add_f32 v[78:79], v[78:79], v[30:31]
	global_store_dwordx4 v59, v[76:79], s[10:11] offset:0 sc0 sc1
	s_waitcnt vmcnt(23)
	v_pk_add_f32 v[80:81], v[80:81], v[32:33]
	v_pk_add_f32 v[82:83], v[82:83], v[34:35]
	global_store_dwordx4 v56, v[80:83], s[10:11] offset:64 sc0 sc1
	s_waitcnt vmcnt(23)
	v_pk_add_f32 v[84:85], v[84:85], v[36:37]
	v_pk_add_f32 v[86:87], v[86:87], v[38:39]
	global_store_dwordx4 v57, v[84:87], s[10:11] offset:64 sc0 sc1
	s_waitcnt vmcnt(23)
	v_pk_add_f32 v[88:89], v[88:89], v[40:41]
	v_pk_add_f32 v[90:91], v[90:91], v[42:43]
	global_store_dwordx4 v58, v[88:91], s[10:11] offset:64 sc0 sc1
	s_waitcnt vmcnt(23)
	v_pk_add_f32 v[92:93], v[92:93], v[44:45]
	v_pk_add_f32 v[94:95], v[94:95], v[46:47]
	global_store_dwordx4 v59, v[92:95], s[10:11] offset:64 sc0 sc1
	s_waitcnt vmcnt(23)
	v_pk_add_f32 v[96:97], v[96:97], v[48:49]
	v_pk_add_f32 v[98:99], v[98:99], v[50:51]
	global_store_dwordx4 v56, v[96:99], s[10:11] offset:128 sc0 sc1
	s_waitcnt vmcnt(23)
	v_pk_add_f32 v[100:101], v[100:101], v[52:53]
	v_pk_add_f32 v[102:103], v[102:103], v[54:55]
	global_store_dwordx4 v57, v[100:103], s[10:11] offset:128 sc0 sc1
	s_waitcnt vmcnt(23)
	v_pk_add_f32 v[104:105], v[104:105], v[240:241]
	v_pk_add_f32 v[106:107], v[106:107], v[242:243]
	global_store_dwordx4 v58, v[104:107], s[10:11] offset:128 sc0 sc1
	s_waitcnt vmcnt(23)
	v_pk_add_f32 v[108:109], v[108:109], v[244:245]
	v_pk_add_f32 v[110:111], v[110:111], v[246:247]
	global_store_dwordx4 v59, v[108:111], s[10:11] offset:128 sc0 sc1
	s_waitcnt vmcnt(23)
	v_pk_add_f32 v[112:113], v[112:113], v[248:249]
	v_pk_add_f32 v[114:115], v[114:115], v[250:251]
	global_store_dwordx4 v56, v[112:115], s[10:11] offset:192 sc0 sc1
	s_waitcnt vmcnt(23)
	v_pk_add_f32 v[116:117], v[116:117], v[252:253]
	v_pk_add_f32 v[118:119], v[118:119], v[254:255]
	global_store_dwordx4 v57, v[116:119], s[10:11] offset:192 sc0 sc1
	s_waitcnt vmcnt(23)
	v_pk_add_f32 v[120:121], v[120:121], v[160:161]
	v_pk_add_f32 v[122:123], v[122:123], v[162:163]
	global_store_dwordx4 v58, v[120:123], s[10:11] offset:192 sc0 sc1
	s_waitcnt vmcnt(23)
	v_pk_add_f32 v[124:125], v[124:125], v[164:165]
	v_pk_add_f32 v[126:127], v[126:127], v[166:167]
	global_store_dwordx4 v59, v[124:127], s[10:11] offset:192 sc0 sc1
	s_waitcnt vmcnt(23)
	v_pk_add_f32 v[128:129], v[128:129], v[168:169]
	v_pk_add_f32 v[130:131], v[130:131], v[170:171]
	global_store_dwordx4 v56, v[128:131], s[10:11] offset:256 sc0 sc1
	s_waitcnt vmcnt(23)
	v_pk_add_f32 v[132:133], v[132:133], v[172:173]
	v_pk_add_f32 v[134:135], v[134:135], v[174:175]
	global_store_dwordx4 v57, v[132:135], s[10:11] offset:256 sc0 sc1
	s_waitcnt vmcnt(23)
	v_pk_add_f32 v[136:137], v[136:137], v[176:177]
	v_pk_add_f32 v[138:139], v[138:139], v[178:179]
	global_store_dwordx4 v58, v[136:139], s[10:11] offset:256 sc0 sc1
	s_waitcnt vmcnt(23)
	v_pk_add_f32 v[140:141], v[140:141], v[180:181]
	v_pk_add_f32 v[142:143], v[142:143], v[182:183]
	global_store_dwordx4 v59, v[140:143], s[10:11] offset:256 sc0 sc1
	s_waitcnt vmcnt(23)
	v_pk_add_f32 v[144:145], v[144:145], v[184:185]
	v_pk_add_f32 v[146:147], v[146:147], v[186:187]
	global_store_dwordx4 v56, v[144:147], s[10:11] offset:320 sc0 sc1
	s_waitcnt vmcnt(23)
	v_pk_add_f32 v[148:149], v[148:149], v[188:189]
	v_pk_add_f32 v[150:151], v[150:151], v[190:191]
	global_store_dwordx4 v57, v[148:151], s[10:11] offset:320 sc0 sc1
	s_waitcnt vmcnt(23)
	v_pk_add_f32 v[152:153], v[152:153], v[192:193]
	v_pk_add_f32 v[154:155], v[154:155], v[194:195]
	global_store_dwordx4 v58, v[152:155], s[10:11] offset:320 sc0 sc1
	s_waitcnt vmcnt(23)
	v_pk_add_f32 v[156:157], v[156:157], v[196:197]
	v_pk_add_f32 v[158:159], v[158:159], v[198:199]
	global_store_dwordx4 v59, v[156:159], s[10:11] offset:320 sc0 sc1
